# baseline (speedup 1.0000x reference)
_ZN3att10attn64_fwdEPKDF16_S1_S1_PDF16_S2_P15HIP_vector_typeIfLj2EEPiPKfS2_:
	s_bitcmp1_b32 s2, 3
	s_cbranch_scc0 .Lattn_noprio
	s_setprio 1
